# speedup vs baseline: 1.0109x; 1.0072x over previous
_ZN4attn11attn_kernelEPKDF16_S1_S1_PDF16_PKyPKh:
	s_cmpk_lt_u32 s2, 0x100
	s_cbranch_scc0 .Lattn_done
	s_mov_b64 s[54:55], s[0:1]
	s_mov_b32 s53, s2
	s_mov_b32 s56, 0
	v_mov_b32_e32 v223, v0

.LBB1_1:
	v_lshlrev_b32_e32 v50, 1, v0
	v_and_b32_e32 v185, 32, v50
	v_lshlrev_b32_e32 v50, 4, v0
	v_and_b32_e32 v50, 0xc0, v50
	v_lshl_or_b32 v203, v200, 8, v50
	v_max_f32_e32 v50, v35, v35
	v_max_f32_e32 v51, v34, v34
	v_max_f32_e32 v50, v51, v50
	s_nop 2
	v_max3_f32 v51, v36, v37, v19
	v_max3_f32 v50, v50, v18, v20
	v_max3_f32 v50, v50, v21, v38
	v_max3_f32 v51, v51, v40, v41
	v_max3_f32 v50, v50, v39, v22
	v_max3_f32 v51, v51, v24, v25
	v_max3_f32 v50, v50, v23, v42
	v_max3_f32 v51, v51, v44, v45
	v_max3_f32 v50, v50, v43, v26
	v_max3_f32 v51, v51, v28, v29
	v_max3_f32 v50, v50, v27, v46
	v_max3_f32 v51, v51, v48, v49
	v_max3_f32 v50, v50, v47, v30
	v_max3_f32 v51, v51, v32, v33
	v_max3_f32 v50, v50, v31, v51
	s_lshl_b64 s[4:5], s[0:1], 10
	s_lshl_b32 s0, s20, 2
	v_mov_b32_e32 v51, v50
	s_and_b32 s31, s0, 0xffffff00
	s_nop 0
	v_permlane32_swap_b32_e32 v50, v51
	s_mov_b32 s0, 0xc6800000
	v_max3_f32 v205, v50, v51, s0
	v_sub_f32_e32 v18, v18, v205
	v_exp_f32_e32 v50, v18
	v_sub_f32_e32 v18, v35, v205
	v_exp_f32_e32 v67, v18
	v_sub_f32_e32 v18, v19, v205
	v_exp_f32_e32 v51, v18
	v_sub_f32_e32 v18, v36, v205
	v_exp_f32_e32 v68, v18
	v_sub_f32_e32 v18, v20, v205
	v_exp_f32_e32 v52, v18
	v_sub_f32_e32 v18, v37, v205
	v_exp_f32_e32 v69, v18
	v_sub_f32_e32 v18, v21, v205
	v_exp_f32_e32 v53, v18
	v_sub_f32_e32 v18, v38, v205
	v_exp_f32_e32 v70, v18
	v_sub_f32_e32 v18, v22, v205
	v_exp_f32_e32 v54, v18
	v_sub_f32_e32 v18, v39, v205
	v_exp_f32_e32 v71, v18
	v_sub_f32_e32 v18, v23, v205
	v_exp_f32_e32 v55, v18
	v_sub_f32_e32 v18, v40, v205
	v_exp_f32_e32 v72, v18
	v_sub_f32_e32 v18, v24, v205
	v_exp_f32_e32 v56, v18
	v_sub_f32_e32 v18, v41, v205
	v_exp_f32_e32 v73, v18
	v_sub_f32_e32 v18, v25, v205
	v_exp_f32_e32 v57, v18
	v_sub_f32_e32 v18, v42, v205
	v_exp_f32_e32 v74, v18
	v_sub_f32_e32 v18, v26, v205
	v_exp_f32_e32 v58, v18
	v_sub_f32_e32 v18, v43, v205
	v_exp_f32_e32 v75, v18
	v_sub_f32_e32 v18, v27, v205
	v_exp_f32_e32 v59, v18
	v_sub_f32_e32 v18, v44, v205
	v_exp_f32_e32 v76, v18
	v_sub_f32_e32 v18, v28, v205
	v_exp_f32_e32 v60, v18
	v_sub_f32_e32 v18, v45, v205
	v_exp_f32_e32 v77, v18
	v_sub_f32_e32 v18, v29, v205
	v_exp_f32_e32 v61, v18
	v_sub_f32_e32 v18, v46, v205
	v_exp_f32_e32 v78, v18
	v_sub_f32_e32 v18, v30, v205
	v_exp_f32_e32 v62, v18
	v_sub_f32_e32 v18, v47, v205
	v_exp_f32_e32 v79, v18
	v_sub_f32_e32 v18, v31, v205
	v_sub_f32_e32 v34, v34, v205
	v_exp_f32_e32 v63, v18
	v_sub_f32_e32 v18, v48, v205
	v_exp_f32_e32 v66, v34
	v_exp_f32_e32 v80, v18
	v_sub_f32_e32 v18, v32, v205
	v_xor_b32_e32 v34, 0x80000000, v205
	v_exp_f32_e32 v64, v18
	v_sub_f32_e32 v18, v49, v205
	v_mov_b32_e32 v35, v34
	v_mov_b32_e32 v36, v34
	v_mov_b32_e32 v37, v34
	v_mov_b32_e32 v38, v34
	v_mov_b32_e32 v39, v34
	v_mov_b32_e32 v40, v34
	v_mov_b32_e32 v41, v34
	v_mov_b32_e32 v42, v34
	v_mov_b32_e32 v43, v34
	v_mov_b32_e32 v44, v34
	v_mov_b32_e32 v45, v34
	v_mov_b32_e32 v46, v34
	v_mov_b32_e32 v47, v34
	v_mov_b32_e32 v48, v34
	v_mov_b32_e32 v49, v34
	v_exp_f32_e32 v81, v18
	v_sub_f32_e32 v18, v33, v205
	s_waitcnt vmcnt(0) lgkmcnt(0)
	s_barrier
	s_mov_b64 s[12:13], 0x60000
	v_exp_f32_e32 v65, v18
	v_lshl_add_u64 v[18:19], v[82:83], 0, s[12:13]
	s_mov_b32 s0, m0
	s_mov_b32 m0, s34
	s_nop 0
	global_load_lds_dwordx4 v[18:19], off
	s_mov_b32 m0, s0
	s_lshl_b32 s21, s21, 1
	s_add_i32 s0, s34, 0x8000
	s_and_b32 s30, s21, 0x780
	s_and_b32 s21, s24, 0x3ffffff0
	s_add_u32 s21, s21, s30
	v_lshl_add_u64 v[18:19], v[190:191], 0, s[18:19]
	s_mov_b32 s1, m0
	s_mov_b32 m0, s0
	s_nop 0
	global_load_lds_dwordx4 v[18:19], off
	s_mov_b32 m0, s1
	s_addc_u32 s25, 0, 0
	ds_read_b128 v[174:177], v206 offset:8192
	ds_read_b128 v[170:173], v206 offset:8704
	ds_read_b128 v[166:169], v206 offset:10240
	ds_read_b128 v[162:165], v206 offset:10752
	ds_read_b128 v[158:161], v206 offset:12288
	ds_read_b128 v[154:157], v206 offset:12800
	ds_read_b128 v[150:153], v206 offset:14336
	ds_read_b128 v[146:149], v206 offset:14848
	s_add_u32 s24, s21, s2
	s_addc_u32 s25, s25, s3
	v_lshl_add_u64 v[18:19], s[24:25], 0, v[188:189]
	v_lshl_add_u64 v[194:195], s[6:7], 0, v[18:19]
	s_or_b32 s6, s2, s30
	s_add_u32 s6, s6, s14
	v_and_b32_e32 v0, 3, v0
	s_addc_u32 s7, s3, 0
	v_lshl_or_b32 v18, v0, 4, s6
	s_lshl_b32 s6, s20, 9
	s_and_b32 s6, s6, 0x18000
	v_mov_b32_e32 v19, s7
	v_lshl_or_b32 v188, v1, 11, s6
	s_waitcnt vmcnt(2) lgkmcnt(0)
	s_barrier
	v_lshl_add_u64 v[0:1], v[18:19], 0, v[188:189]
	v_lshl_add_u64 v[198:199], s[8:9], 0, v[0:1]
	v_mov_b64_e32 v[32:33], v[16:17]
	v_or3_b32 v207, v185, v202, v203
	v_cmp_gt_u32_e64 s[0:1], 32, v182
	v_lshl_or_b32 v204, v201, 2, s31
	v_lshl_add_u64 v[192:193], v[190:191], 0, s[16:17]
	v_lshl_add_u64 v[196:197], v[194:195], 0, s[18:19]
	v_lshl_add_u64 v[0:1], v[198:199], 0, s[18:19]
	s_mov_b32 s24, 0x41000000
	s_mov_b64 s[6:7], 0x80000
	v_mov_b32_e32 v188, 0xceabfb8f
	v_mov_b64_e32 v[30:31], v[14:15]
	v_mov_b64_e32 v[28:29], v[12:13]
	v_mov_b64_e32 v[26:27], v[10:11]
	v_mov_b64_e32 v[24:25], v[8:9]
	v_mov_b64_e32 v[22:23], v[6:7]
	v_mov_b64_e32 v[20:21], v[4:5]
	v_mov_b64_e32 v[18:19], v[2:3]
	s_mov_b32 s14, 0
	v_readfirstlane_b32 s44, v196
	v_readfirstlane_b32 s45, v197
	v_readfirstlane_b32 s46, v192
	v_readfirstlane_b32 s47, v193
	s_nop 1
	v_subrev_u32_e32 v220, s44, v196
	v_subrev_u32_e32 v221, s46, v192
	s_nop 1
	s_add_u32 s44, s44, 0x60000
	s_addc_u32 s45, s45, 0
.LBB1_2:
	s_add_i32 s25, s26, 2
	v_add_u32_e32 v208, s14, v207
	ds_read_b64_tr_b16 v[178:179], v208 offset:24576
	ds_read_b64_tr_b16 v[180:181], v208 offset:25088
	s_waitcnt lgkmcnt(9)
	v_mfma_f32_32x32x16_f16 v[98:113], v[174:177], v[138:141], v[34:49]
	v_add_f32_e32 v82, v66, v67
	v_add_f32_e32 v82, v68, v82
	v_add_f32_e32 v82, v69, v82
	v_add_f32_e32 v82, v70, v82
	v_add_f32_e32 v82, v71, v82
	v_cvt_pk_f16_f32 v142, v66, v67
	v_cvt_pk_f16_f32 v143, v68, v69
	ds_read_b64_tr_b16 v[174:175], v208 offset:28672
	ds_read_b64_tr_b16 v[176:177], v208 offset:29184
	v_add_f32_e32 v66, v72, v82
	s_waitcnt lgkmcnt(10)
	v_mfma_f32_32x32x16_f16 v[82:97], v[170:173], v[138:141], v[34:49]
	v_add_f32_e32 v66, v73, v66
	v_add_f32_e32 v66, v74, v66
	v_add_f32_e32 v66, v75, v66
	v_cvt_pk_f16_f32 v144, v70, v71
	v_cvt_pk_f16_f32 v145, v72, v73
	ds_read_b64_tr_b16 v[170:171], v208 offset:25600
	ds_read_b64_tr_b16 v[172:173], v208 offset:26112
	s_waitcnt lgkmcnt(11)
	v_mfma_f32_32x32x16_f16 v[98:113], v[166:169], v[130:133], v[98:113]
	v_add_f32_e32 v66, v76, v66
	v_add_f32_e32 v66, v77, v66
	v_add_f32_e32 v66, v78, v66
	v_add_f32_e32 v66, v79, v66
	v_cvt_pk_f16_f32 v134, v74, v75
	v_cvt_pk_f16_f32 v135, v76, v77
	ds_read_b64_tr_b16 v[74:75], v208 offset:29696
	ds_read_b64_tr_b16 v[76:77], v208 offset:30208
	s_waitcnt lgkmcnt(12)
	v_mfma_f32_32x32x16_f16 v[82:97], v[162:165], v[130:133], v[82:97]
	v_add_f32_e32 v66, v80, v66
	v_add_f32_e32 v66, v81, v66
	v_add_f32_e32 v66, v50, v66
	v_add_f32_e32 v66, v51, v66
	v_cvt_pk_f16_f32 v136, v78, v79
	v_cvt_pk_f16_f32 v137, v80, v81
	ds_read_b64_tr_b16 v[70:71], v208 offset:26624
	ds_read_b64_tr_b16 v[72:73], v208 offset:27136
	s_waitcnt lgkmcnt(13)
	v_mfma_f32_32x32x16_f16 v[98:113], v[158:161], v[126:129], v[98:113]
	v_add_f32_e32 v66, v52, v66
	v_add_f32_e32 v66, v53, v66
	v_add_f32_e32 v66, v54, v66
	v_add_f32_e32 v78, v55, v66
	v_cvt_pk_f16_f32 v122, v50, v51
	v_cvt_pk_f16_f32 v123, v52, v53
	ds_read_b64_tr_b16 v[66:67], v208 offset:30720
	ds_read_b64_tr_b16 v[68:69], v208 offset:31232
	s_waitcnt lgkmcnt(14)
	v_mfma_f32_32x32x16_f16 v[82:97], v[154:157], v[126:129], v[82:97]
	v_add_f32_e32 v50, v56, v78
	v_add_f32_e32 v50, v57, v50
	v_add_f32_e32 v50, v58, v50
	v_add_f32_e32 v50, v59, v50
	v_cvt_pk_f16_f32 v124, v54, v55
	v_cvt_pk_f16_f32 v125, v56, v57
	ds_read_b64_tr_b16 v[54:55], v208 offset:27648
	ds_read_b64_tr_b16 v[56:57], v208 offset:28160
	s_waitcnt lgkmcnt(14)
	v_mfma_f32_32x32x16_f16 v[98:113], v[150:153], v[118:121], v[98:113]
	v_add_f32_e32 v50, v60, v50
	v_add_f32_e32 v50, v61, v50
	v_add_f32_e32 v50, v62, v50
	v_add_f32_e32 v78, v63, v50
	v_cvt_pk_f16_f32 v114, v58, v59
	v_cvt_pk_f16_f32 v115, v60, v61
	ds_read_b64_tr_b16 v[50:51], v208 offset:31744
	ds_read_b64_tr_b16 v[52:53], v208 offset:32256
	v_mfma_f32_32x32x16_f16 v[82:97], v[146:149], v[118:121], v[82:97]
	v_add_f32_e32 v58, v64, v78
	v_add_f32_e32 v78, v65, v58
	v_cvt_pk_f16_f32 v116, v62, v63
	v_cvt_pk_f16_f32 v117, v64, v65
	s_add_i32 s14, s27, s34
	s_mov_b32 m0, s14
	s_nop 0
	global_load_lds_dwordx4 v220, s[44:45]
	s_add_u32 s44, s44, 0x20000
	s_addc_u32 s45, s45, 0
	s_add_i32 s14, s23, s35
	s_mov_b32 m0, s14
	s_nop 0
	global_load_lds_dwordx4 v221, s[46:47]
	s_add_u32 s46, s46, 0x20000
	s_addc_u32 s47, s47, 0
	s_lshr_b32 s37, s33, s25
	s_bitcmp0_b32 s37, 0
	s_cbranch_scc0 .LBB1_12
.LBB1_3:
	v_max_f32_e32 v58, v98, v99
	v_max3_f32 v59, v100, v101, v83
	v_max3_f32 v58, v58, v82, v84
	v_max3_f32 v58, v58, v85, v102
	v_max3_f32 v59, v59, v104, v105
	v_max3_f32 v58, v58, v103, v86
	v_max3_f32 v59, v59, v88, v89
	v_max3_f32 v58, v58, v87, v106
	v_max3_f32 v59, v59, v108, v109
	v_max3_f32 v58, v58, v107, v90
	v_max3_f32 v59, v59, v92, v93
	v_max3_f32 v58, v58, v91, v110
	v_max3_f32 v59, v59, v112, v113
	v_max3_f32 v58, v58, v111, v94
	v_max3_f32 v59, v59, v96, v97
	v_max3_f32 v58, v58, v95, v59
	v_cmp_lt_f32_e32 vcc, s24, v58
	s_cmp_lg_u64 vcc, 0
	v_add_f32_e32 v189, v189, v78
	s_cselect_b64 s[18:19], -1, 0
	s_cbranch_vccnz .LBB1_13

.LBB1_6:
	s_add_i32 s14, s23, 0x2000
	s_cmpk_lg_i32 s23, 0x4000
	s_cselect_b32 s36, s14, 0
	v_add_u32_e32 v208, s27, v207
	ds_read_b64_tr_b16 v[154:155], v208 offset:24576
	ds_read_b64_tr_b16 v[156:157], v208 offset:25088
	s_waitcnt lgkmcnt(9)
	v_mfma_f32_32x32x16_f16 v[66:81], v[58:61], v[138:141], v[34:49]
	v_add_f32_e32 v50, v98, v99
	v_add_f32_e32 v50, v100, v50
	v_add_f32_e32 v50, v101, v50
	v_add_f32_e32 v50, v102, v50
	v_add_f32_e32 v50, v103, v50
	v_cvt_pk_f16_f32 v142, v98, v99
	v_cvt_pk_f16_f32 v143, v100, v101
	ds_read_b64_tr_b16 v[150:151], v208 offset:28672
	ds_read_b64_tr_b16 v[152:153], v208 offset:29184
	v_add_f32_e32 v50, v104, v50
	v_add_f32_e32 v50, v105, v50
	v_add_f32_e32 v50, v106, v50
	v_add_f32_e32 v98, v107, v50
	s_waitcnt lgkmcnt(10)
	v_mfma_f32_32x32x16_f16 v[50:65], v[146:149], v[138:141], v[34:49]
	v_cvt_pk_f16_f32 v144, v102, v103
	v_cvt_pk_f16_f32 v145, v104, v105
	ds_read_b64_tr_b16 v[146:147], v208 offset:25600
	ds_read_b64_tr_b16 v[148:149], v208 offset:26112
	s_waitcnt lgkmcnt(11)
	v_mfma_f32_32x32x16_f16 v[66:81], v[178:181], v[130:133], v[66:81]
	v_add_f32_e32 v98, v108, v98
	v_add_f32_e32 v98, v109, v98
	v_add_f32_e32 v98, v110, v98
	v_add_f32_e32 v98, v111, v98
	v_cvt_pk_f16_f32 v134, v106, v107
	v_cvt_pk_f16_f32 v135, v108, v109
	ds_read_b64_tr_b16 v[106:107], v208 offset:29696
	ds_read_b64_tr_b16 v[108:109], v208 offset:30208
	s_waitcnt lgkmcnt(12)
	v_mfma_f32_32x32x16_f16 v[50:65], v[170:173], v[130:133], v[50:65]
	v_add_f32_e32 v98, v112, v98
	v_add_f32_e32 v98, v113, v98
	v_add_f32_e32 v98, v82, v98
	v_add_f32_e32 v98, v83, v98
	v_cvt_pk_f16_f32 v136, v110, v111
	v_cvt_pk_f16_f32 v137, v112, v113
	ds_read_b64_tr_b16 v[102:103], v208 offset:26624
	ds_read_b64_tr_b16 v[104:105], v208 offset:27136
	s_waitcnt lgkmcnt(13)
	v_mfma_f32_32x32x16_f16 v[66:81], v[174:177], v[126:129], v[66:81]
	v_add_f32_e32 v98, v84, v98
	v_add_f32_e32 v98, v85, v98
	v_add_f32_e32 v98, v86, v98
	v_add_f32_e32 v110, v87, v98
	v_cvt_pk_f16_f32 v122, v82, v83
	v_cvt_pk_f16_f32 v123, v84, v85
	ds_read_b64_tr_b16 v[98:99], v208 offset:30720
	ds_read_b64_tr_b16 v[100:101], v208 offset:31232
	s_waitcnt lgkmcnt(14)
	v_mfma_f32_32x32x16_f16 v[50:65], v[162:165], v[126:129], v[50:65]
	v_add_f32_e32 v82, v88, v110
	v_add_f32_e32 v82, v89, v82
	v_add_f32_e32 v82, v90, v82
	v_add_f32_e32 v82, v91, v82
	v_cvt_pk_f16_f32 v124, v86, v87
	v_cvt_pk_f16_f32 v125, v88, v89
	ds_read_b64_tr_b16 v[86:87], v208 offset:27648
	ds_read_b64_tr_b16 v[88:89], v208 offset:28160
	s_waitcnt lgkmcnt(14)
	v_mfma_f32_32x32x16_f16 v[66:81], v[166:169], v[118:121], v[66:81]
	v_add_f32_e32 v82, v92, v82
	v_add_f32_e32 v82, v93, v82
	v_add_f32_e32 v82, v94, v82
	v_add_f32_e32 v110, v95, v82
	v_cvt_pk_f16_f32 v114, v90, v91
	v_cvt_pk_f16_f32 v115, v92, v93
	ds_read_b64_tr_b16 v[82:83], v208 offset:31744
	ds_read_b64_tr_b16 v[84:85], v208 offset:32256
	v_mfma_f32_32x32x16_f16 v[50:65], v[158:161], v[118:121], v[50:65]
	v_add_f32_e32 v90, v96, v110
	v_add_f32_e32 v110, v97, v90
	v_cvt_pk_f16_f32 v116, v94, v95
	v_cvt_pk_f16_f32 v117, v96, v97
	s_add_i32 s14, s23, s34
	s_mov_b32 m0, s14
	s_nop 0
	global_load_lds_dwordx4 v220, s[44:45]
	s_add_u32 s44, s44, 0x20000
	s_addc_u32 s45, s45, 0
	s_add_i32 s14, s36, s35
	s_mov_b32 m0, s14
	s_nop 0
	global_load_lds_dwordx4 v221, s[46:47]
	s_add_u32 s46, s46, 0x20000
	s_addc_u32 s47, s47, 0
	s_bitcmp0_b32 s37, 1
	s_cbranch_scc0 .LBB1_16
.LBB1_7:
	v_max_f32_e32 v90, v66, v67
	v_max3_f32 v91, v68, v69, v51
	v_max3_f32 v90, v90, v50, v52
	v_max3_f32 v90, v90, v53, v70
	v_max3_f32 v91, v91, v72, v73
	v_max3_f32 v90, v90, v71, v54
	v_max3_f32 v91, v91, v56, v57
	v_max3_f32 v90, v90, v55, v74
	v_max3_f32 v91, v91, v76, v77
	v_max3_f32 v90, v90, v75, v58
	v_max3_f32 v91, v91, v60, v61
	v_max3_f32 v90, v90, v59, v78
	v_max3_f32 v91, v91, v80, v81
	v_max3_f32 v90, v90, v79, v62
	v_max3_f32 v91, v91, v64, v65
	v_max3_f32 v90, v90, v63, v91
	v_cmp_lt_f32_e32 vcc, s24, v90
	s_cmp_lg_u64 vcc, 0
	v_add_f32_e32 v189, v189, v110
	s_cselect_b64 s[18:19], -1, 0
	s_cbranch_vccnz .LBB1_17

.LBB1_10:
	s_add_i32 s14, s36, 0x2000
	s_cmpk_lg_i32 s36, 0x4000
	s_cselect_b32 s18, s14, 0
	s_add_i32 s22, s22, 32
	s_cmp_lt_u32 s25, 25
	s_cbranch_scc0 .LBB1_20
	s_mov_b32 s26, s25
	s_mov_b32 s14, s23
	s_mov_b32 s27, s36
	s_mov_b32 s23, s18
	s_branch .LBB1_2

.LBB1_13:
	v_mov_b32_e32 v59, v58
	s_nop 1
	v_permlane32_swap_b32_e32 v58, v59
	v_max_f32_e32 v58, v58, v59
	v_max_f32_e32 v34, v58, v58
	v_max_f32_e32 v58, 0, v34
	v_exp_f32_e64 v59, -v58
	v_add_f32_e32 v205, v205, v58
	v_xor_b32_e32 v34, 0x80000000, v205
	v_mov_b32_e32 v35, v34
	v_mov_b32_e32 v36, v34
	v_mov_b32_e32 v37, v34
	v_mov_b32_e32 v38, v34
	v_mov_b32_e32 v39, v34
	v_mov_b32_e32 v40, v34
	v_mov_b32_e32 v41, v34
	v_mov_b32_e32 v42, v34
	v_mov_b32_e32 v43, v34
	v_mov_b32_e32 v44, v34
	v_mov_b32_e32 v45, v34
	v_mov_b32_e32 v46, v34
	v_mov_b32_e32 v47, v34
	v_mov_b32_e32 v48, v34
	v_mov_b32_e32 v49, v34
	s_and_saveexec_b64 s[20:21], s[0:1]
	ds_write_b32 v204, v59 offset:49152
	s_or_b64 exec, exec, s[20:21]
	v_sub_f32_e32 v113, v113, v58
	v_sub_f32_e32 v112, v112, v58
	v_sub_f32_e32 v111, v111, v58
	v_sub_f32_e32 v110, v110, v58
	v_sub_f32_e32 v109, v109, v58
	v_sub_f32_e32 v108, v108, v58
	v_sub_f32_e32 v107, v107, v58
	v_sub_f32_e32 v106, v106, v58
	v_sub_f32_e32 v105, v105, v58
	v_sub_f32_e32 v104, v104, v58
	v_sub_f32_e32 v103, v103, v58
	v_sub_f32_e32 v102, v102, v58
	v_sub_f32_e32 v101, v101, v58
	v_sub_f32_e32 v100, v100, v58
	v_sub_f32_e32 v99, v99, v58
	v_sub_f32_e32 v98, v98, v58
	v_sub_f32_e32 v97, v97, v58
	v_sub_f32_e32 v96, v96, v58
	v_sub_f32_e32 v95, v95, v58
	v_sub_f32_e32 v94, v94, v58
	v_sub_f32_e32 v93, v93, v58
	v_sub_f32_e32 v92, v92, v58
	v_sub_f32_e32 v91, v91, v58
	v_sub_f32_e32 v90, v90, v58
	v_sub_f32_e32 v89, v89, v58
	v_sub_f32_e32 v88, v88, v58
	v_sub_f32_e32 v87, v87, v58
	v_sub_f32_e32 v86, v86, v58
	v_sub_f32_e32 v85, v85, v58
	v_sub_f32_e32 v84, v84, v58
	v_sub_f32_e32 v83, v83, v58
	v_sub_f32_e32 v82, v82, v58
	v_mul_f32_e32 v189, v189, v59
	s_branch .LBB1_4

.LBB1_17:
	v_mov_b32_e32 v91, v90
	s_nop 1
	v_permlane32_swap_b32_e32 v90, v91
	v_max_f32_e32 v90, v90, v91
	v_max_f32_e32 v34, v90, v90
	v_max_f32_e32 v90, 0, v34
	v_exp_f32_e64 v91, -v90
	v_add_f32_e32 v205, v205, v90
	v_xor_b32_e32 v34, 0x80000000, v205
	v_mov_b32_e32 v35, v34
	v_mov_b32_e32 v36, v34
	v_mov_b32_e32 v37, v34
	v_mov_b32_e32 v38, v34
	v_mov_b32_e32 v39, v34
	v_mov_b32_e32 v40, v34
	v_mov_b32_e32 v41, v34
	v_mov_b32_e32 v42, v34
	v_mov_b32_e32 v43, v34
	v_mov_b32_e32 v44, v34
	v_mov_b32_e32 v45, v34
	v_mov_b32_e32 v46, v34
	v_mov_b32_e32 v47, v34
	v_mov_b32_e32 v48, v34
	v_mov_b32_e32 v49, v34
	s_and_saveexec_b64 s[20:21], s[0:1]
	ds_write_b32 v204, v91 offset:49152
	s_or_b64 exec, exec, s[20:21]
	v_sub_f32_e32 v81, v81, v90
	v_sub_f32_e32 v80, v80, v90
	v_sub_f32_e32 v79, v79, v90
	v_sub_f32_e32 v78, v78, v90
	v_sub_f32_e32 v77, v77, v90
	v_sub_f32_e32 v76, v76, v90
	v_sub_f32_e32 v75, v75, v90
	v_sub_f32_e32 v74, v74, v90
	v_sub_f32_e32 v73, v73, v90
	v_sub_f32_e32 v72, v72, v90
	v_sub_f32_e32 v71, v71, v90
	v_sub_f32_e32 v70, v70, v90
	v_sub_f32_e32 v69, v69, v90
	v_sub_f32_e32 v68, v68, v90
	v_sub_f32_e32 v67, v67, v90
	v_sub_f32_e32 v66, v66, v90
	v_sub_f32_e32 v65, v65, v90
	v_sub_f32_e32 v64, v64, v90
	v_sub_f32_e32 v63, v63, v90
	v_sub_f32_e32 v62, v62, v90
	v_sub_f32_e32 v61, v61, v90
	v_sub_f32_e32 v60, v60, v90
	v_sub_f32_e32 v59, v59, v90
	v_sub_f32_e32 v58, v58, v90
	v_sub_f32_e32 v57, v57, v90
	v_sub_f32_e32 v56, v56, v90
	v_sub_f32_e32 v55, v55, v90
	v_sub_f32_e32 v54, v54, v90
	v_sub_f32_e32 v53, v53, v90
	v_sub_f32_e32 v52, v52, v90
	v_sub_f32_e32 v51, v51, v90
	v_sub_f32_e32 v50, v50, v90
	v_mul_f32_e32 v189, v189, v91
	s_branch .LBB1_8

.LBB1_58:
	s_lshl_b64 s[0:1], s[4:5], 1
	s_add_u32 s0, s10, s0
	s_addc_u32 s1, s11, s1
	s_lshl_b32 s2, s29, 12
	v_lshlrev_b32_e32 v0, 9, v200
	v_or3_b32 v0, s2, v0, v50
	v_fma_mixlo_f16 v1, v18, v69, 0
	ds_write_b16 v0, v1 offset:51200
	v_fma_mixlo_f16 v1, v2, v69, 0
	ds_write_b16 v0, v1 offset:51264
	v_fma_mixlo_f16 v1, v19, v68, 0
	ds_write_b16 v0, v1 offset:51328
	v_fma_mixlo_f16 v1, v3, v68, 0
	ds_write_b16 v0, v1 offset:51392
	v_fma_mixlo_f16 v1, v20, v67, 0
	ds_write_b16 v0, v1 offset:51456
	v_fma_mixlo_f16 v1, v4, v67, 0
	ds_write_b16 v0, v1 offset:51520
	v_fma_mixlo_f16 v1, v21, v66, 0
	ds_write_b16 v0, v1 offset:51584
	v_fma_mixlo_f16 v1, v5, v66, 0
	ds_write_b16 v0, v1 offset:51648
	v_fma_mixlo_f16 v1, v22, v64, 0
	ds_write_b16 v0, v1 offset:52224
	v_fma_mixlo_f16 v1, v6, v64, 0
	ds_write_b16 v0, v1 offset:52288
	v_fma_mixlo_f16 v1, v23, v65, 0
	ds_write_b16 v0, v1 offset:52352
	v_fma_mixlo_f16 v1, v7, v65, 0
	ds_write_b16 v0, v1 offset:52416
	v_fma_mixlo_f16 v1, v24, v63, 0
	ds_write_b16 v0, v1 offset:52480
	v_fma_mixlo_f16 v1, v8, v63, 0
	ds_write_b16 v0, v1 offset:52544
	v_fma_mixlo_f16 v1, v25, v61, 0
	ds_write_b16 v0, v1 offset:52608
	v_fma_mixlo_f16 v1, v9, v61, 0
	ds_write_b16 v0, v1 offset:52672
	v_fma_mixlo_f16 v1, v26, v62, 0
	ds_write_b16 v0, v1 offset:53248
	v_fma_mixlo_f16 v1, v10, v62, 0
	ds_write_b16 v0, v1 offset:53312
	v_fma_mixlo_f16 v1, v27, v60, 0
	ds_write_b16 v0, v1 offset:53376
	v_fma_mixlo_f16 v1, v11, v60, 0
	ds_write_b16 v0, v1 offset:53440
	v_fma_mixlo_f16 v1, v28, v59, 0
	ds_write_b16 v0, v1 offset:53504
	v_fma_mixlo_f16 v1, v12, v59, 0
	ds_write_b16 v0, v1 offset:53568
	v_fma_mixlo_f16 v1, v29, v58, 0
	ds_write_b16 v0, v1 offset:53632
	v_fma_mixlo_f16 v1, v13, v58, 0
	ds_write_b16 v0, v1 offset:53696
	v_fma_mixlo_f16 v1, v30, v57, 0
	ds_write_b16 v0, v1 offset:54272
	v_fma_mixlo_f16 v1, v14, v57, 0
	ds_write_b16 v0, v1 offset:54336
	v_fma_mixlo_f16 v1, v31, v56, 0
	ds_write_b16 v0, v1 offset:54400
	v_fma_mixlo_f16 v1, v15, v56, 0
	ds_write_b16 v0, v1 offset:54464
	v_fma_mixlo_f16 v1, v32, v55, 0
	ds_write_b16 v0, v1 offset:54528
	v_fma_mixlo_f16 v1, v16, v55, 0
	ds_write_b16 v0, v1 offset:54592
	v_fma_mixlo_f16 v1, v33, v54, 0
	ds_write_b16 v0, v1 offset:54656
	v_fma_mixlo_f16 v1, v17, v54, 0
	ds_write_b16 v0, v1 offset:54720
	v_and_b32_e32 v0, 56, v183
	v_lshlrev_b32_e32 v8, 1, v0
	v_lshrrev_b32_e32 v14, 3, v182
	v_or_b32_e32 v15, s2, v8
	s_waitcnt lgkmcnt(0)
	v_lshl_or_b32 v0, v14, 7, v15
	v_or_b32_e32 v16, 8, v14
	ds_read_b128 v[0:3], v0 offset:51200
	v_lshl_or_b32 v4, v16, 7, v15
	s_add_u32 s0, s0, s28
	ds_read_b128 v[4:7], v4 offset:51200
	s_addc_u32 s1, s1, 0
	v_mov_b32_e32 v9, 0
	v_lshl_add_u64 v[10:11], s[0:1], 0, v[8:9]
	v_lshlrev_b32_e32 v8, 11, v14
	v_lshl_add_u64 v[12:13], v[10:11], 0, v[8:9]
	v_lshlrev_b32_e32 v8, 11, v16
	s_waitcnt lgkmcnt(1)
	global_store_dwordx4 v[12:13], v[0:3], off
	s_nop 1
	v_lshl_add_u64 v[0:1], v[10:11], 0, v[8:9]
	s_waitcnt lgkmcnt(0)
	global_store_dwordx4 v[0:1], v[4:7], off
	s_nop 1
	v_or_b32_e32 v4, 16, v14
	v_lshl_or_b32 v0, v4, 7, v15
	v_or_b32_e32 v14, 24, v14
	ds_read_b128 v[0:3], v0 offset:51200
	v_lshlrev_b32_e32 v8, 11, v4
	v_lshl_or_b32 v4, v14, 7, v15
	ds_read_b128 v[4:7], v4 offset:51200
	v_lshl_add_u64 v[12:13], v[10:11], 0, v[8:9]
	v_lshlrev_b32_e32 v8, 11, v14
	s_waitcnt lgkmcnt(1)
	global_store_dwordx4 v[12:13], v[0:3], off
	s_nop 1
	v_lshl_add_u64 v[0:1], v[10:11], 0, v[8:9]
	s_waitcnt lgkmcnt(0)
	global_store_dwordx4 v[0:1], v[4:7], off
	s_waitcnt lgkmcnt(0)
	s_barrier
	s_cmp_lg_u32 s56, 0
	s_cbranch_scc1 .Lattn_done
	s_mov_b32 s56, 1
	s_mov_b64 s[0:1], s[54:55]
	s_add_i32 s2, s53, 0x100
	v_mov_b32_e32 v0, v223
	s_mov_b64 exec, -1
	s_branch .Lattn_again

	.amdhsa_kernel _ZN4attn11attn_kernelEPKDF16_S1_S1_PDF16_PKyPKh
		.amdhsa_group_segment_fixed_size 83968
		.amdhsa_private_segment_fixed_size 0
		.amdhsa_kernarg_size 48
		.amdhsa_user_sgpr_count 2
		.amdhsa_user_sgpr_dispatch_ptr 0
		.amdhsa_user_sgpr_queue_ptr 0
		.amdhsa_user_sgpr_kernarg_segment_ptr 1
		.amdhsa_user_sgpr_dispatch_id 0
		.amdhsa_user_sgpr_kernarg_preload_length 0
		.amdhsa_user_sgpr_kernarg_preload_offset 0
		.amdhsa_user_sgpr_private_segment_size 0
		.amdhsa_uses_dynamic_stack 0
		.amdhsa_enable_private_segment 0
		.amdhsa_system_sgpr_workgroup_id_x 1
		.amdhsa_system_sgpr_workgroup_id_y 0
		.amdhsa_system_sgpr_workgroup_id_z 0
		.amdhsa_system_sgpr_workgroup_info 0
		.amdhsa_system_vgpr_workitem_id 0
		.amdhsa_next_free_vgpr 224
		.amdhsa_next_free_sgpr 96
		.amdhsa_accum_offset 224
		.amdhsa_reserve_vcc 1
		.amdhsa_float_round_mode_32 0
		.amdhsa_float_round_mode_16_64 0
		.amdhsa_float_denorm_mode_32 3
		.amdhsa_float_denorm_mode_16_64 3
		.amdhsa_dx10_clamp 1
		.amdhsa_ieee_mode 1
		.amdhsa_fp16_overflow 0
		.amdhsa_tg_split 0
		.amdhsa_exception_fp_ieee_invalid_op 0
		.amdhsa_exception_fp_denorm_src 0
		.amdhsa_exception_fp_ieee_div_zero 0
		.amdhsa_exception_fp_ieee_overflow 0
		.amdhsa_exception_fp_ieee_underflow 0
		.amdhsa_exception_fp_ieee_inexact 0
		.amdhsa_exception_int_div_zero 0
	.end_amdhsa_kernel

amdhsa.kernels:
  - .agpr_count:     0
    .args:
      - .offset:         0
        .size:           64
        .value_kind:     by_value
    .group_segment_fixed_size: 0
    .kernarg_segment_align: 8
    .kernarg_segment_size: 64
    .language:       OpenCL C
    .language_version:
      - 2
      - 0
    .max_flat_workgroup_size: 256
    .name:           _Z11prep_kernel8PrepArgs
    .private_segment_fixed_size: 0
    .sgpr_count:     22
    .sgpr_spill_count: 0
    .symbol:         _Z11prep_kernel8PrepArgs.kd
    .uniform_work_group_size: 1
    .uses_dynamic_stack: false
    .vgpr_count:     38
    .vgpr_spill_count: 0
    .wavefront_size: 64
  - .agpr_count:     0
    .args:
      - .address_space:  global
        .offset:         0
        .size:           8
        .value_kind:     global_buffer
      - .address_space:  global
        .offset:         8
        .size:           8
        .value_kind:     global_buffer
      - .address_space:  global
        .offset:         16
        .size:           8
        .value_kind:     global_buffer
      - .address_space:  global
        .offset:         24
        .size:           8
        .value_kind:     global_buffer
      - .address_space:  global
        .offset:         32
        .size:           8
        .value_kind:     global_buffer
      - .address_space:  global
        .offset:         40
        .size:           8
        .value_kind:     global_buffer
    .group_segment_fixed_size: 83968
    .kernarg_segment_align: 8
    .kernarg_segment_size: 48
    .language:       OpenCL C
    .language_version:
      - 2
      - 0
    .max_flat_workgroup_size: 512
    .name:           _ZN4attn11attn_kernelEPKDF16_S1_S1_PDF16_PKyPKh
    .private_segment_fixed_size: 0
    .sgpr_count:     48
    .sgpr_spill_count: 0
    .symbol:         _ZN4attn11attn_kernelEPKDF16_S1_S1_PDF16_PKyPKh.kd
    .uniform_work_group_size: 1
    .uses_dynamic_stack: false
    .vgpr_count:     224
    .vgpr_spill_count: 0
    .wavefront_size: 64
  - .agpr_count:     0
    .args:
      - .offset:         0
        .size:           120
        .value_kind:     by_value
      - .offset:         120
        .size:           4
        .value_kind:     hidden_block_count_x
      - .offset:         124
        .size:           4
        .value_kind:     hidden_block_count_y
      - .offset:         128
        .size:           4
        .value_kind:     hidden_block_count_z
      - .offset:         132
        .size:           2
        .value_kind:     hidden_group_size_x
      - .offset:         134
        .size:           2
        .value_kind:     hidden_group_size_y
      - .offset:         136
        .size:           2
        .value_kind:     hidden_group_size_z
      - .offset:         138
        .size:           2
        .value_kind:     hidden_remainder_x
      - .offset:         140
        .size:           2
        .value_kind:     hidden_remainder_y
      - .offset:         142
        .size:           2
        .value_kind:     hidden_remainder_z
      - .offset:         160
        .size:           8
        .value_kind:     hidden_global_offset_x
      - .offset:         168
        .size:           8
        .value_kind:     hidden_global_offset_y
      - .offset:         176
        .size:           8
        .value_kind:     hidden_global_offset_z
      - .offset:         184
        .size:           2
        .value_kind:     hidden_grid_dims
    .group_segment_fixed_size: 131072
    .kernarg_segment_align: 8
    .kernarg_segment_size: 376
    .language:       OpenCL C
    .language_version:
      - 2
      - 0
    .max_flat_workgroup_size: 512
    .name:           _ZN4gemm15gemm128r_kernelILb1ELi0ELi3ELb1EEEvNS_7Args128E
    .private_segment_fixed_size: 0
    .sgpr_count:     104
    .sgpr_spill_count: 0
    .symbol:         _ZN4gemm15gemm128r_kernelILb1ELi0ELi3ELb1EEEvNS_7Args128E.kd
    .uniform_work_group_size: 1
    .uses_dynamic_stack: false
    .vgpr_count:     211
    .vgpr_spill_count: 0
    .wavefront_size: 64
  - .agpr_count:     0
    .args:
      - .offset:         0
        .size:           120
        .value_kind:     by_value
      - .offset:         120
        .size:           4
        .value_kind:     hidden_block_count_x
      - .offset:         124
        .size:           4
        .value_kind:     hidden_block_count_y
      - .offset:         128
        .size:           4
        .value_kind:     hidden_block_count_z
      - .offset:         132
        .size:           2
        .value_kind:     hidden_group_size_x
      - .offset:         134
        .size:           2
        .value_kind:     hidden_group_size_y
      - .offset:         136
        .size:           2
        .value_kind:     hidden_group_size_z
      - .offset:         138
        .size:           2
        .value_kind:     hidden_remainder_x
      - .offset:         140
        .size:           2
        .value_kind:     hidden_remainder_y
      - .offset:         142
        .size:           2
        .value_kind:     hidden_remainder_z
      - .offset:         160
        .size:           8
        .value_kind:     hidden_global_offset_x
      - .offset:         168
        .size:           8
        .value_kind:     hidden_global_offset_y
      - .offset:         176
        .size:           8
        .value_kind:     hidden_global_offset_z
      - .offset:         184
        .size:           2
        .value_kind:     hidden_grid_dims
    .group_segment_fixed_size: 131072
    .kernarg_segment_align: 8
    .kernarg_segment_size: 376
    .language:       OpenCL C
    .language_version:
      - 2
      - 0
    .max_flat_workgroup_size: 512
    .name:           _ZN4gemm15gemm128r_kernelILb0ELi1ELi1ELb0EEEvNS_7Args128E
    .private_segment_fixed_size: 0
    .sgpr_count:     75
    .sgpr_spill_count: 0
    .symbol:         _ZN4gemm15gemm128r_kernelILb0ELi1ELi1ELb0EEEvNS_7Args128E.kd
    .uniform_work_group_size: 1
    .uses_dynamic_stack: false
    .vgpr_count:     178
    .vgpr_spill_count: 0
    .wavefront_size: 64
